# prologue transposed weight copies: the wait before an item's LDS transposition no longer drains the next item's loads (vmcnt(8)), the next item is waited (vmcnt(4)) before the register hand-over; on t
# baseline (speedup 1.0000x reference)
.LBB0_114:
	s_or_b64 exec, exec, s[8:9]
	s_waitcnt vmcnt(8)
	s_branch .Ltrw_115

.Ltrw_115:
	ds_write2_b32 v75, v2, v3 offset1:1
	ds_write2_b32 v75, v4, v5 offset0:2 offset1:3
	v_add_u32_e32 v2, 0x420, v75
	ds_write2_b32 v2, v6, v7 offset1:1
	v_add_u32_e32 v2, 0x428, v75
	ds_write2_b32 v2, v8, v9 offset1:1
	v_add_u32_e32 v2, 0x840, v75
	ds_write2_b32 v2, v10, v11 offset1:1
	v_add_u32_e32 v2, 0x848, v75
	ds_write2_b32 v2, v12, v13 offset1:1
	v_add_u32_e32 v2, 0xc60, v75
	ds_write2_b32 v2, v14, v15 offset1:1
	v_add_u32_e32 v2, 0xc68, v75
	s_ashr_i32 s4, s16, 31
	ds_write2_b32 v2, v16, v17 offset1:1
	v_add_u32_e32 v2, 0x1080, v75
	s_lshr_b32 s4, s4, 23
	ds_write2_b32 v2, v18, v19 offset1:1
	v_add_u32_e32 v2, 0x1088, v75
	s_add_i32 s4, s16, s4
	ds_write2_b32 v2, v20, v21 offset1:1
	v_add_u32_e32 v2, 0x14a0, v75
	s_ashr_i32 s5, s4, 9
	s_and_b32 s4, s4, 0xfe00
	ds_write2_b32 v2, v22, v23 offset1:1
	v_add_u32_e32 v2, 0x14a8, v75
	s_sub_i32 s4, s16, s4
	s_mul_hi_i32 s8, s5, 0xa00000
	s_mul_i32 s5, s5, 0xa00000
	ds_write2_b32 v2, v24, v25 offset1:1
	v_add_u32_e32 v2, 0x18c0, v75
	s_add_u32 s9, s10, s5
	s_sext_i32_i16 s5, s4
	ds_write2_b32 v2, v38, v39 offset1:1
	v_add_u32_e32 v2, 0x18c8, v75
	s_addc_u32 s8, s11, s8
	s_bfe_u32 s5, s5, 0x60019
	ds_write2_b32 v2, v40, v41 offset1:1
	v_add_u32_e32 v2, 0x1ce0, v75
	s_add_i32 s5, s4, s5
	ds_write2_b32 v2, v42, v43 offset1:1
	v_add_u32_e32 v2, 0x1ce8, v75
	s_sext_i32_i16 s16, s5
	s_and_b32 s5, s5, 0xffc0
	ds_write2_b32 v2, v44, v45 offset1:1
	s_sub_i32 s4, s4, s5
	s_waitcnt lgkmcnt(0)
	s_sext_i32_i16 s18, s4
	s_and_b32 s4, s16, 0xffffffc0
	s_ashr_i32 s5, s4, 31
	ds_read2_b32 v[6:7], v74 offset0:33 offset1:41
	ds_read2_b32 v[8:9], v74 offset1:8
	ds_read2_b32 v[10:11], v74 offset0:66 offset1:74
	ds_read2_b32 v[12:13], v74 offset0:99 offset1:107
	ds_read2_b32 v[14:15], v74 offset0:132 offset1:140
	ds_read2_b32 v[16:17], v74 offset0:165 offset1:173
	ds_read2_b32 v[18:19], v74 offset0:198 offset1:206
	ds_read2_b32 v[20:21], v74 offset0:231 offset1:239
	s_lshl_b64 s[4:5], s[4:5], 1
	s_add_u32 s4, s9, s4
	v_lshl_add_u32 v24, s18, 5, v72
	s_addc_u32 s5, s8, s5
	v_ashrrev_i32_e32 v25, 31, v24
	v_lshl_add_u64 v[22:23], s[4:5], 0, v[66:67]
	v_lshlrev_b64 v[38:39], 10, v[24:25]
	s_waitcnt lgkmcnt(6)
	v_cvt_pk_bf16_f32 v2, v8, v6
	s_waitcnt lgkmcnt(4)
	v_cvt_pk_bf16_f32 v3, v10, v12
	s_waitcnt lgkmcnt(2)
	v_cvt_pk_bf16_f32 v4, v14, v16
	s_waitcnt lgkmcnt(0)
	v_cvt_pk_bf16_f32 v5, v18, v20
	v_lshl_add_u64 v[38:39], v[22:23], 0, v[38:39]
	v_add_u32_e32 v6, 8, v24
	global_store_dwordx4 v[38:39], v[2:5], off
	s_andn2_b64 vcc, exec, s[6:7]
	s_mov_b32 s16, s17
	v_cvt_pk_bf16_f32 v2, v9, v7
	v_ashrrev_i32_e32 v7, 31, v6
	v_cvt_pk_bf16_f32 v3, v11, v13
	v_cvt_pk_bf16_f32 v4, v15, v17
	v_cvt_pk_bf16_f32 v5, v19, v21
	v_lshlrev_b64 v[6:7], 10, v[6:7]
	ds_read2_b32 v[8:9], v74 offset0:49 offset1:57
	ds_read2_b32 v[10:11], v74 offset0:16 offset1:24
	ds_read2_b32 v[12:13], v74 offset0:82 offset1:90
	ds_read2_b32 v[14:15], v74 offset0:115 offset1:123
	ds_read2_b32 v[16:17], v74 offset0:148 offset1:156
	ds_read2_b32 v[18:19], v74 offset0:181 offset1:189
	ds_read2_b32 v[20:21], v74 offset0:214 offset1:222
	ds_read2_b32 v[38:39], v74 offset0:247 offset1:255
	v_lshl_add_u64 v[6:7], v[22:23], 0, v[6:7]
	global_store_dwordx4 v[6:7], v[2:5], off
	v_add_u32_e32 v6, 16, v24
	v_ashrrev_i32_e32 v7, 31, v6
	v_lshlrev_b64 v[6:7], 10, v[6:7]
	s_waitcnt lgkmcnt(6)
	v_cvt_pk_bf16_f32 v2, v10, v8
	s_waitcnt lgkmcnt(4)
	v_cvt_pk_bf16_f32 v3, v12, v14
	s_waitcnt lgkmcnt(2)
	v_cvt_pk_bf16_f32 v4, v16, v18
	s_waitcnt lgkmcnt(0)
	v_cvt_pk_bf16_f32 v5, v20, v38
	v_lshl_add_u64 v[6:7], v[22:23], 0, v[6:7]
	global_store_dwordx4 v[6:7], v[2:5], off
	v_add_u32_e32 v6, 24, v24
	v_ashrrev_i32_e32 v7, 31, v6
	v_lshlrev_b64 v[6:7], 10, v[6:7]
	v_cvt_pk_bf16_f32 v2, v11, v9
	v_cvt_pk_bf16_f32 v3, v13, v15
	v_cvt_pk_bf16_f32 v4, v17, v19
	v_cvt_pk_bf16_f32 v5, v21, v39
	v_lshl_add_u64 v[6:7], v[22:23], 0, v[6:7]
	global_store_dwordx4 v[6:7], v[2:5], off
	s_waitcnt lgkmcnt(0)
	s_waitcnt vmcnt(4)
	v_mov_b32_e32 v6, v34
	v_mov_b32_e32 v7, v35
	v_mov_b32_e32 v2, v30
	v_mov_b32_e32 v3, v31
	v_mov_b32_e32 v4, v32
	v_mov_b32_e32 v5, v33
	v_mov_b32_e32 v8, v36
	v_mov_b32_e32 v9, v37
	v_mov_b32_e32 v10, v26
	v_mov_b32_e32 v11, v27
	v_mov_b32_e32 v12, v28
	v_mov_b32_e32 v13, v29
	v_mov_b32_e32 v14, v46
	v_mov_b32_e32 v15, v47
	v_mov_b32_e32 v16, v48
	v_mov_b32_e32 v17, v49
	v_mov_b32_e32 v18, v54
	v_mov_b32_e32 v19, v55
	v_mov_b32_e32 v20, v56
	v_mov_b32_e32 v21, v57
	v_mov_b32_e32 v22, v58
	v_mov_b32_e32 v23, v59
	v_mov_b32_e32 v24, v60
	v_mov_b32_e32 v25, v61
	v_mov_b32_e32 v38, v50
	v_mov_b32_e32 v39, v51
	v_mov_b32_e32 v40, v52
	v_mov_b32_e32 v41, v53
	v_mov_b32_e32 v42, v62
	v_mov_b32_e32 v43, v63
	v_mov_b32_e32 v44, v64
	v_mov_b32_e32 v45, v65
	s_cbranch_vccz .LBB0_125

.Ltrw_138:
	ds_write2_b32 v75, v2, v3 offset1:1
	ds_write2_b32 v75, v4, v5 offset0:2 offset1:3
	v_add_u32_e32 v2, 0x420, v75
	ds_write2_b32 v2, v6, v7 offset1:1
	v_add_u32_e32 v2, 0x428, v75
	ds_write2_b32 v2, v8, v9 offset1:1
	v_add_u32_e32 v2, 0x840, v75
	ds_write2_b32 v2, v10, v11 offset1:1
	v_add_u32_e32 v2, 0x848, v75
	ds_write2_b32 v2, v12, v13 offset1:1
	v_add_u32_e32 v2, 0xc60, v75
	s_ashr_i32 s4, s16, 31
	ds_write2_b32 v2, v14, v15 offset1:1
	v_add_u32_e32 v2, 0xc68, v75
	s_lshr_b32 s4, s4, 20
	ds_write2_b32 v2, v16, v17 offset1:1
	v_add_u32_e32 v2, 0x1080, v75
	s_add_i32 s5, s16, s4
	ds_write2_b32 v2, v18, v19 offset1:1
	v_add_u32_e32 v2, 0x1088, v75
	s_ashr_i32 s4, s5, 12
	s_and_b32 s5, s5, 0xf000
	ds_write2_b32 v2, v20, v21 offset1:1
	v_add_u32_e32 v2, 0x14a0, v75
	s_sub_i32 s8, s16, s5
	s_ashr_i32 s5, s4, 31
	ds_write2_b32 v2, v22, v23 offset1:1
	v_add_u32_e32 v2, 0x14a8, v75
	s_lshl_b64 s[4:5], s[4:5], 24
	ds_write2_b32 v2, v24, v25 offset1:1
	v_add_u32_e32 v2, 0x18c0, v75
	s_add_u32 s9, s10, s4
	s_sext_i32_i16 s4, s8
	ds_write2_b32 v2, v38, v39 offset1:1
	v_add_u32_e32 v2, 0x18c8, v75
	s_addc_u32 s16, s11, s5
	s_bfe_u32 s4, s4, 0x60019
	ds_write2_b32 v2, v40, v41 offset1:1
	v_add_u32_e32 v2, 0x1ce0, v75
	s_add_i32 s4, s8, s4
	ds_write2_b32 v2, v42, v43 offset1:1
	v_add_u32_e32 v2, 0x1ce8, v75
	s_sext_i32_i16 s5, s4
	s_and_b32 s4, s4, 0xffc0
	ds_write2_b32 v2, v44, v45 offset1:1
	s_sub_i32 s4, s8, s4
	s_waitcnt lgkmcnt(0)
	s_sext_i32_i16 s8, s4
	s_and_b32 s4, s5, 0xffffffc0
	s_ashr_i32 s5, s4, 31
	ds_read2_b32 v[6:7], v74 offset0:33 offset1:41
	ds_read2_b32 v[8:9], v74 offset1:8
	ds_read2_b32 v[10:11], v74 offset0:66 offset1:74
	ds_read2_b32 v[12:13], v74 offset0:99 offset1:107
	ds_read2_b32 v[14:15], v74 offset0:132 offset1:140
	ds_read2_b32 v[16:17], v74 offset0:165 offset1:173
	ds_read2_b32 v[18:19], v74 offset0:198 offset1:206
	ds_read2_b32 v[20:21], v74 offset0:231 offset1:239
	s_lshl_b64 s[4:5], s[4:5], 1
	s_add_u32 s4, s9, s4
	v_lshl_add_u32 v24, s8, 5, v72
	s_addc_u32 s5, s16, s5
	v_ashrrev_i32_e32 v25, 31, v24
	v_lshl_add_u64 v[22:23], s[4:5], 0, v[66:67]
	v_lshlrev_b64 v[38:39], 13, v[24:25]
	s_waitcnt lgkmcnt(6)
	v_cvt_pk_bf16_f32 v2, v8, v6
	s_waitcnt lgkmcnt(4)
	v_cvt_pk_bf16_f32 v3, v10, v12
	s_waitcnt lgkmcnt(2)
	v_cvt_pk_bf16_f32 v4, v14, v16
	s_waitcnt lgkmcnt(0)
	v_cvt_pk_bf16_f32 v5, v18, v20
	v_lshl_add_u64 v[38:39], v[22:23], 0, v[38:39]
	v_add_u32_e32 v6, 8, v24
	global_store_dwordx4 v[38:39], v[2:5], off
	s_andn2_b64 vcc, exec, s[6:7]
	s_mov_b32 s16, s17
	v_cvt_pk_bf16_f32 v2, v9, v7
	v_ashrrev_i32_e32 v7, 31, v6
	v_cvt_pk_bf16_f32 v3, v11, v13
	v_cvt_pk_bf16_f32 v4, v15, v17
	v_cvt_pk_bf16_f32 v5, v19, v21
	v_lshlrev_b64 v[6:7], 13, v[6:7]
	ds_read2_b32 v[8:9], v74 offset0:49 offset1:57
	ds_read2_b32 v[10:11], v74 offset0:16 offset1:24
	ds_read2_b32 v[12:13], v74 offset0:82 offset1:90
	ds_read2_b32 v[14:15], v74 offset0:115 offset1:123
	ds_read2_b32 v[16:17], v74 offset0:148 offset1:156
	ds_read2_b32 v[18:19], v74 offset0:181 offset1:189
	ds_read2_b32 v[20:21], v74 offset0:214 offset1:222
	ds_read2_b32 v[38:39], v74 offset0:247 offset1:255
	v_lshl_add_u64 v[6:7], v[22:23], 0, v[6:7]
	global_store_dwordx4 v[6:7], v[2:5], off
	v_add_u32_e32 v6, 16, v24
	v_ashrrev_i32_e32 v7, 31, v6
	v_lshlrev_b64 v[6:7], 13, v[6:7]
	s_waitcnt lgkmcnt(6)
	v_cvt_pk_bf16_f32 v2, v10, v8
	s_waitcnt lgkmcnt(4)
	v_cvt_pk_bf16_f32 v3, v12, v14
	s_waitcnt lgkmcnt(2)
	v_cvt_pk_bf16_f32 v4, v16, v18
	s_waitcnt lgkmcnt(0)
	v_cvt_pk_bf16_f32 v5, v20, v38
	v_lshl_add_u64 v[6:7], v[22:23], 0, v[6:7]
	global_store_dwordx4 v[6:7], v[2:5], off
	v_add_u32_e32 v6, 24, v24
	v_ashrrev_i32_e32 v7, 31, v6
	v_lshlrev_b64 v[6:7], 13, v[6:7]
	v_cvt_pk_bf16_f32 v2, v11, v9
	v_cvt_pk_bf16_f32 v3, v13, v15
	v_cvt_pk_bf16_f32 v4, v17, v19
	v_cvt_pk_bf16_f32 v5, v21, v39
	v_lshl_add_u64 v[6:7], v[22:23], 0, v[6:7]
	global_store_dwordx4 v[6:7], v[2:5], off
	s_waitcnt lgkmcnt(0)
	s_waitcnt vmcnt(4)
	v_mov_b32_e32 v6, v34
	v_mov_b32_e32 v7, v35
	v_mov_b32_e32 v2, v30
	v_mov_b32_e32 v3, v31
	v_mov_b32_e32 v4, v32
	v_mov_b32_e32 v5, v33
	v_mov_b32_e32 v8, v36
	v_mov_b32_e32 v9, v37
	v_mov_b32_e32 v10, v26
	v_mov_b32_e32 v11, v27
	v_mov_b32_e32 v12, v28
	v_mov_b32_e32 v13, v29
	v_mov_b32_e32 v14, v46
	v_mov_b32_e32 v15, v47
	v_mov_b32_e32 v16, v48
	v_mov_b32_e32 v17, v49
	v_mov_b32_e32 v18, v54
	v_mov_b32_e32 v19, v55
	v_mov_b32_e32 v20, v56
	v_mov_b32_e32 v21, v57
	v_mov_b32_e32 v22, v58
	v_mov_b32_e32 v23, v59
	v_mov_b32_e32 v24, v60
	v_mov_b32_e32 v25, v61
	v_mov_b32_e32 v38, v50
	v_mov_b32_e32 v39, v51
	v_mov_b32_e32 v40, v52
	v_mov_b32_e32 v41, v53
	v_mov_b32_e32 v42, v62
	v_mov_b32_e32 v43, v63
	v_mov_b32_e32 v44, v64
	v_mov_b32_e32 v45, v65
	s_cbranch_vccz .LBB0_148

.LBB0_160:
	s_or_b64 exec, exec, s[6:7]
	s_waitcnt vmcnt(8)
	s_branch .Ltrw_161

.Ltrw_161:
	ds_write2_b32 v73, v2, v3 offset1:1
	ds_write2_b32 v73, v4, v5 offset0:2 offset1:3
	v_add_u32_e32 v2, 0x420, v73
	ds_write2_b32 v2, v6, v7 offset1:1
	v_add_u32_e32 v2, 0x428, v73
	ds_write2_b32 v2, v8, v9 offset1:1
	v_add_u32_e32 v2, 0x840, v73
	ds_write2_b32 v2, v10, v11 offset1:1
	v_add_u32_e32 v2, 0x848, v73
	ds_write2_b32 v2, v12, v13 offset1:1
	v_add_u32_e32 v2, 0xc60, v73
	ds_write2_b32 v2, v14, v15 offset1:1
	v_add_u32_e32 v2, 0xc68, v73
	s_mul_hi_i32 s6, s15, 0x2aaaaaab
	ds_write2_b32 v2, v16, v17 offset1:1
	v_add_u32_e32 v2, 0x1080, v73
	s_lshr_b32 s7, s6, 31
	s_ashr_i32 s6, s6, 10
	ds_write2_b32 v2, v18, v19 offset1:1
	v_add_u32_e32 v2, 0x1088, v73
	s_add_i32 s6, s6, s7
	ds_write2_b32 v2, v20, v21 offset1:1
	v_add_u32_e32 v2, 0x14a0, v73
	s_mul_i32 s7, s6, 0xffffe800
	ds_write2_b32 v2, v22, v23 offset1:1
	v_add_u32_e32 v2, 0x14a8, v73
	s_add_i32 s7, s15, s7
	s_mul_hi_i32 s15, s6, 0x1800000
	s_mul_i32 s6, s6, 0x1800000
	ds_write2_b32 v2, v24, v25 offset1:1
	v_add_u32_e32 v2, 0x18c0, v73
	s_add_u32 s17, s8, s6
	s_mul_i32 s6, s7, 0x2aab
	ds_write2_b32 v2, v38, v39 offset1:1
	v_add_u32_e32 v2, 0x18c8, v73
	s_addc_u32 s15, s9, s15
	s_lshr_b32 s18, s6, 31
	s_ashr_i32 s6, s6, 21
	ds_write2_b32 v2, v40, v41 offset1:1
	v_add_u32_e32 v2, 0x1ce0, v73
	s_add_i32 s6, s6, s18
	ds_write2_b32 v2, v42, v43 offset1:1
	v_add_u32_e32 v2, 0x1ce8, v73
	s_sext_i32_i16 s18, s6
	s_mulk_i32 s6, 0xc0
	ds_write2_b32 v2, v44, v45 offset1:1
	s_sub_i32 s6, s7, s6
	s_waitcnt lgkmcnt(0)
	s_sext_i32_i16 s19, s6
	s_lshl_b32 s6, s18, 6
	s_ashr_i32 s7, s6, 31
	ds_read2_b32 v[6:7], v71 offset0:33 offset1:41
	ds_read2_b32 v[8:9], v71 offset1:8
	ds_read2_b32 v[10:11], v71 offset0:66 offset1:74
	ds_read2_b32 v[12:13], v71 offset0:99 offset1:107
	ds_read2_b32 v[14:15], v71 offset0:132 offset1:140
	ds_read2_b32 v[16:17], v71 offset0:165 offset1:173
	ds_read2_b32 v[18:19], v71 offset0:198 offset1:206
	ds_read2_b32 v[20:21], v71 offset0:231 offset1:239
	s_lshl_b64 s[6:7], s[6:7], 1
	s_add_u32 s6, s17, s6
	v_lshl_add_u32 v24, s19, 5, v72
	s_addc_u32 s7, s15, s7
	v_ashrrev_i32_e32 v25, 31, v24
	v_lshl_add_u64 v[22:23], s[6:7], 0, v[66:67]
	v_lshlrev_b64 v[38:39], 12, v[24:25]
	s_waitcnt lgkmcnt(6)
	v_cvt_pk_bf16_f32 v2, v8, v6
	s_waitcnt lgkmcnt(4)
	v_cvt_pk_bf16_f32 v3, v10, v12
	s_waitcnt lgkmcnt(2)
	v_cvt_pk_bf16_f32 v4, v14, v16
	s_waitcnt lgkmcnt(0)
	v_cvt_pk_bf16_f32 v5, v18, v20
	v_lshl_add_u64 v[38:39], v[22:23], 0, v[38:39]
	v_add_u32_e32 v6, 8, v24
	global_store_dwordx4 v[38:39], v[2:5], off
	s_andn2_b64 vcc, exec, s[4:5]
	s_mov_b32 s15, s16
	v_cvt_pk_bf16_f32 v2, v9, v7
	v_ashrrev_i32_e32 v7, 31, v6
	v_cvt_pk_bf16_f32 v3, v11, v13
	v_cvt_pk_bf16_f32 v4, v15, v17
	v_cvt_pk_bf16_f32 v5, v19, v21
	v_lshlrev_b64 v[6:7], 12, v[6:7]
	ds_read2_b32 v[8:9], v71 offset0:49 offset1:57
	ds_read2_b32 v[10:11], v71 offset0:16 offset1:24
	ds_read2_b32 v[12:13], v71 offset0:82 offset1:90
	ds_read2_b32 v[14:15], v71 offset0:115 offset1:123
	ds_read2_b32 v[16:17], v71 offset0:148 offset1:156
	ds_read2_b32 v[18:19], v71 offset0:181 offset1:189
	ds_read2_b32 v[20:21], v71 offset0:214 offset1:222
	ds_read2_b32 v[38:39], v71 offset0:247 offset1:255
	v_lshl_add_u64 v[6:7], v[22:23], 0, v[6:7]
	global_store_dwordx4 v[6:7], v[2:5], off
	v_add_u32_e32 v6, 16, v24
	v_ashrrev_i32_e32 v7, 31, v6
	v_lshlrev_b64 v[6:7], 12, v[6:7]
	s_waitcnt lgkmcnt(6)
	v_cvt_pk_bf16_f32 v2, v10, v8
	s_waitcnt lgkmcnt(4)
	v_cvt_pk_bf16_f32 v3, v12, v14
	s_waitcnt lgkmcnt(2)
	v_cvt_pk_bf16_f32 v4, v16, v18
	s_waitcnt lgkmcnt(0)
	v_cvt_pk_bf16_f32 v5, v20, v38
	v_lshl_add_u64 v[6:7], v[22:23], 0, v[6:7]
	global_store_dwordx4 v[6:7], v[2:5], off
	v_add_u32_e32 v6, 24, v24
	v_ashrrev_i32_e32 v7, 31, v6
	v_lshlrev_b64 v[6:7], 12, v[6:7]
	v_cvt_pk_bf16_f32 v2, v11, v9
	v_cvt_pk_bf16_f32 v3, v13, v15
	v_cvt_pk_bf16_f32 v4, v17, v19
	v_cvt_pk_bf16_f32 v5, v21, v39
	v_lshl_add_u64 v[6:7], v[22:23], 0, v[6:7]
	global_store_dwordx4 v[6:7], v[2:5], off
	s_waitcnt lgkmcnt(0)
	s_waitcnt vmcnt(4)
	v_mov_b32_e32 v6, v34
	v_mov_b32_e32 v7, v35
	v_mov_b32_e32 v2, v30
	v_mov_b32_e32 v3, v31
	v_mov_b32_e32 v4, v32
	v_mov_b32_e32 v5, v33
	v_mov_b32_e32 v8, v36
	v_mov_b32_e32 v9, v37
	v_mov_b32_e32 v10, v26
	v_mov_b32_e32 v11, v27
	v_mov_b32_e32 v12, v28
	v_mov_b32_e32 v13, v29
	v_mov_b32_e32 v14, v46
	v_mov_b32_e32 v15, v47
	v_mov_b32_e32 v16, v48
	v_mov_b32_e32 v17, v49
	v_mov_b32_e32 v18, v54
	v_mov_b32_e32 v19, v55
	v_mov_b32_e32 v20, v56
	v_mov_b32_e32 v21, v57
	v_mov_b32_e32 v22, v58
	v_mov_b32_e32 v23, v59
	v_mov_b32_e32 v24, v60
	v_mov_b32_e32 v25, v61
	v_mov_b32_e32 v38, v50
	v_mov_b32_e32 v39, v51
	v_mov_b32_e32 v40, v52
	v_mov_b32_e32 v41, v53
	v_mov_b32_e32 v42, v62
	v_mov_b32_e32 v43, v63
	v_mov_b32_e32 v44, v64
	v_mov_b32_e32 v45, v65
	s_cbranch_vccz .LBB0_171

.Ltrw_184:
	ds_write2_b32 v75, v2, v3 offset1:1
	ds_write2_b32 v75, v4, v5 offset0:2 offset1:3
	v_add_u32_e32 v2, 0x420, v75
	ds_write2_b32 v2, v6, v7 offset1:1
	v_add_u32_e32 v2, 0x428, v75
	ds_write2_b32 v2, v8, v9 offset1:1
	v_add_u32_e32 v2, 0x840, v75
	ds_write2_b32 v2, v10, v11 offset1:1
	v_add_u32_e32 v2, 0x848, v75
	ds_write2_b32 v2, v12, v13 offset1:1
	v_add_u32_e32 v2, 0xc60, v75
	s_ashr_i32 s4, s16, 31
	ds_write2_b32 v2, v14, v15 offset1:1
	v_add_u32_e32 v2, 0xc68, v75
	s_lshr_b32 s4, s4, 21
	ds_write2_b32 v2, v16, v17 offset1:1
	v_add_u32_e32 v2, 0x1080, v75
	s_add_i32 s5, s16, s4
	ds_write2_b32 v2, v18, v19 offset1:1
	v_add_u32_e32 v2, 0x1088, v75
	s_ashr_i32 s4, s5, 11
	s_and_b32 s5, s5, 0xf800
	ds_write2_b32 v2, v20, v21 offset1:1
	v_add_u32_e32 v2, 0x14a0, v75
	s_sub_i32 s8, s16, s5
	s_ashr_i32 s5, s4, 31
	ds_write2_b32 v2, v22, v23 offset1:1
	v_add_u32_e32 v2, 0x14a8, v75
	s_lshl_b64 s[4:5], s[4:5], 23
	ds_write2_b32 v2, v24, v25 offset1:1
	v_add_u32_e32 v2, 0x18c0, v75
	s_add_u32 s9, s10, s4
	s_sext_i32_i16 s4, s8
	ds_write2_b32 v2, v38, v39 offset1:1
	v_add_u32_e32 v2, 0x18c8, v75
	s_addc_u32 s16, s11, s5
	s_bfe_u32 s4, s4, 0x60019
	ds_write2_b32 v2, v40, v41 offset1:1
	v_add_u32_e32 v2, 0x1ce0, v75
	s_add_i32 s4, s8, s4
	ds_write2_b32 v2, v42, v43 offset1:1
	v_add_u32_e32 v2, 0x1ce8, v75
	s_sext_i32_i16 s5, s4
	s_and_b32 s4, s4, 0xffc0
	ds_write2_b32 v2, v44, v45 offset1:1
	s_sub_i32 s4, s8, s4
	s_waitcnt lgkmcnt(0)
	s_sext_i32_i16 s8, s4
	s_and_b32 s4, s5, 0xffffffc0
	s_ashr_i32 s5, s4, 31
	ds_read2_b32 v[6:7], v74 offset0:33 offset1:41
	ds_read2_b32 v[8:9], v74 offset1:8
	ds_read2_b32 v[10:11], v74 offset0:66 offset1:74
	ds_read2_b32 v[12:13], v74 offset0:99 offset1:107
	ds_read2_b32 v[14:15], v74 offset0:132 offset1:140
	ds_read2_b32 v[16:17], v74 offset0:165 offset1:173
	ds_read2_b32 v[18:19], v74 offset0:198 offset1:206
	ds_read2_b32 v[20:21], v74 offset0:231 offset1:239
	s_lshl_b64 s[4:5], s[4:5], 1
	s_add_u32 s4, s9, s4
	v_lshl_add_u32 v24, s8, 5, v72
	s_addc_u32 s5, s16, s5
	v_ashrrev_i32_e32 v25, 31, v24
	v_lshl_add_u64 v[22:23], s[4:5], 0, v[66:67]
	v_lshlrev_b64 v[38:39], 12, v[24:25]
	s_waitcnt lgkmcnt(6)
	v_cvt_pk_bf16_f32 v2, v8, v6
	s_waitcnt lgkmcnt(4)
	v_cvt_pk_bf16_f32 v3, v10, v12
	s_waitcnt lgkmcnt(2)
	v_cvt_pk_bf16_f32 v4, v14, v16
	s_waitcnt lgkmcnt(0)
	v_cvt_pk_bf16_f32 v5, v18, v20
	v_lshl_add_u64 v[38:39], v[22:23], 0, v[38:39]
	v_add_u32_e32 v6, 8, v24
	global_store_dwordx4 v[38:39], v[2:5], off
	s_andn2_b64 vcc, exec, s[6:7]
	s_mov_b32 s16, s17
	v_cvt_pk_bf16_f32 v2, v9, v7
	v_ashrrev_i32_e32 v7, 31, v6
	v_cvt_pk_bf16_f32 v3, v11, v13
	v_cvt_pk_bf16_f32 v4, v15, v17
	v_cvt_pk_bf16_f32 v5, v19, v21
	v_lshlrev_b64 v[6:7], 12, v[6:7]
	ds_read2_b32 v[8:9], v74 offset0:49 offset1:57
	ds_read2_b32 v[10:11], v74 offset0:16 offset1:24
	ds_read2_b32 v[12:13], v74 offset0:82 offset1:90
	ds_read2_b32 v[14:15], v74 offset0:115 offset1:123
	ds_read2_b32 v[16:17], v74 offset0:148 offset1:156
	ds_read2_b32 v[18:19], v74 offset0:181 offset1:189
	ds_read2_b32 v[20:21], v74 offset0:214 offset1:222
	ds_read2_b32 v[38:39], v74 offset0:247 offset1:255
	v_lshl_add_u64 v[6:7], v[22:23], 0, v[6:7]
	global_store_dwordx4 v[6:7], v[2:5], off
	v_add_u32_e32 v6, 16, v24
	v_ashrrev_i32_e32 v7, 31, v6
	v_lshlrev_b64 v[6:7], 12, v[6:7]
	s_waitcnt lgkmcnt(6)
	v_cvt_pk_bf16_f32 v2, v10, v8
	s_waitcnt lgkmcnt(4)
	v_cvt_pk_bf16_f32 v3, v12, v14
	s_waitcnt lgkmcnt(2)
	v_cvt_pk_bf16_f32 v4, v16, v18
	s_waitcnt lgkmcnt(0)
	v_cvt_pk_bf16_f32 v5, v20, v38
	v_lshl_add_u64 v[6:7], v[22:23], 0, v[6:7]
	global_store_dwordx4 v[6:7], v[2:5], off
	v_add_u32_e32 v6, 24, v24
	v_ashrrev_i32_e32 v7, 31, v6
	v_lshlrev_b64 v[6:7], 12, v[6:7]
	v_cvt_pk_bf16_f32 v2, v11, v9
	v_cvt_pk_bf16_f32 v3, v13, v15
	v_cvt_pk_bf16_f32 v4, v17, v19
	v_cvt_pk_bf16_f32 v5, v21, v39
	v_lshl_add_u64 v[6:7], v[22:23], 0, v[6:7]
	global_store_dwordx4 v[6:7], v[2:5], off
	s_waitcnt lgkmcnt(0)
	s_waitcnt vmcnt(4)
	v_mov_b32_e32 v6, v34
	v_mov_b32_e32 v7, v35
	v_mov_b32_e32 v2, v30
	v_mov_b32_e32 v3, v31
	v_mov_b32_e32 v4, v32
	v_mov_b32_e32 v5, v33
	v_mov_b32_e32 v8, v36
	v_mov_b32_e32 v9, v37
	v_mov_b32_e32 v10, v26
	v_mov_b32_e32 v11, v27
	v_mov_b32_e32 v12, v28
	v_mov_b32_e32 v13, v29
	v_mov_b32_e32 v14, v46
	v_mov_b32_e32 v15, v47
	v_mov_b32_e32 v16, v48
	v_mov_b32_e32 v17, v49
	v_mov_b32_e32 v18, v54
	v_mov_b32_e32 v19, v55
	v_mov_b32_e32 v20, v56
	v_mov_b32_e32 v21, v57
	v_mov_b32_e32 v22, v58
	v_mov_b32_e32 v23, v59
	v_mov_b32_e32 v24, v60
	v_mov_b32_e32 v25, v61
	v_mov_b32_e32 v38, v50
	v_mov_b32_e32 v39, v51
	v_mov_b32_e32 v40, v52
	v_mov_b32_e32 v41, v53
	v_mov_b32_e32 v42, v62
	v_mov_b32_e32 v43, v63
	v_mov_b32_e32 v44, v64
	v_mov_b32_e32 v45, v65
	s_cbranch_vccz .LBB0_194

.LBB0_206:
	s_or_b64 exec, exec, s[10:11]
	s_waitcnt vmcnt(8)
	s_branch .Ltrw_207

.Ltrw_207:
	ds_write2_b32 v79, v2, v3 offset1:1
	ds_write2_b32 v79, v4, v5 offset0:2 offset1:3
	v_add_u32_e32 v2, 0x420, v79
	ds_write2_b32 v2, v6, v7 offset1:1
	v_add_u32_e32 v2, 0x428, v79
	ds_write2_b32 v2, v8, v9 offset1:1
	v_add_u32_e32 v2, 0x840, v79
	ds_write2_b32 v2, v10, v11 offset1:1
	v_add_u32_e32 v2, 0x848, v79
	ds_write2_b32 v2, v12, v13 offset1:1
	v_add_u32_e32 v2, 0xc60, v79
	s_ashr_i32 s4, s20, 31
	ds_write2_b32 v2, v14, v15 offset1:1
	v_add_u32_e32 v2, 0xc68, v79
	s_lshr_b32 s4, s4, 19
	ds_write2_b32 v2, v16, v17 offset1:1
	v_add_u32_e32 v2, 0x1080, v79
	s_add_i32 s5, s20, s4
	ds_write2_b32 v2, v18, v19 offset1:1
	v_add_u32_e32 v2, 0x1088, v79
	s_ashr_i32 s4, s5, 13
	s_and_b32 s5, s5, 0xe000
	ds_write2_b32 v2, v20, v21 offset1:1
	v_add_u32_e32 v2, 0x14a0, v79
	s_sub_i32 s10, s20, s5
	s_ashr_i32 s5, s4, 31
	ds_write2_b32 v2, v22, v23 offset1:1
	v_add_u32_e32 v2, 0x14a8, v79
	s_lshl_b64 s[4:5], s[4:5], 25
	ds_write2_b32 v2, v24, v25 offset1:1
	v_add_u32_e32 v2, 0x18c0, v79
	s_add_u32 s11, s17, s4
	s_sext_i32_i16 s4, s10
	ds_write2_b32 v2, v38, v39 offset1:1
	v_add_u32_e32 v2, 0x18c8, v79
	s_addc_u32 s20, s18, s5
	s_bfe_u32 s4, s4, 0x80017
	ds_write2_b32 v2, v40, v41 offset1:1
	v_add_u32_e32 v2, 0x1ce0, v79
	s_add_i32 s4, s10, s4
	ds_write2_b32 v2, v42, v43 offset1:1
	v_add_u32_e32 v2, 0x1ce8, v79
	s_sext_i32_i16 s5, s4
	s_and_b32 s4, s4, 0xff00
	ds_write2_b32 v2, v44, v45 offset1:1
	s_ashr_i32 s5, s5, 8
	s_sub_i32 s4, s10, s4
	s_waitcnt lgkmcnt(0)
	s_sext_i32_i16 s10, s4
	s_lshl_b32 s4, s5, 6
	s_ashr_i32 s5, s4, 31
	ds_read2_b32 v[6:7], v77 offset0:33 offset1:41
	ds_read2_b32 v[8:9], v77 offset1:8
	ds_read2_b32 v[10:11], v77 offset0:66 offset1:74
	ds_read2_b32 v[12:13], v77 offset0:99 offset1:107
	ds_read2_b32 v[14:15], v77 offset0:132 offset1:140
	ds_read2_b32 v[16:17], v77 offset0:165 offset1:173
	ds_read2_b32 v[18:19], v77 offset0:198 offset1:206
	ds_read2_b32 v[20:21], v77 offset0:231 offset1:239
	s_lshl_b32 s10, s10, 5
	s_lshl_b64 s[4:5], s[4:5], 1
	s_add_u32 s4, s11, s4
	v_add_u32_e32 v24, s10, v72
	s_addc_u32 s5, s20, s5
	v_ashrrev_i32_e32 v25, 31, v24
	v_lshl_add_u64 v[22:23], s[4:5], 0, v[66:67]
	v_lshlrev_b64 v[24:25], 12, v[24:25]
	s_waitcnt lgkmcnt(6)
	v_cvt_pk_bf16_f32 v2, v8, v6
	s_waitcnt lgkmcnt(4)
	v_cvt_pk_bf16_f32 v3, v10, v12
	s_waitcnt lgkmcnt(2)
	v_cvt_pk_bf16_f32 v4, v14, v16
	s_waitcnt lgkmcnt(0)
	v_cvt_pk_bf16_f32 v5, v18, v20
	v_lshl_add_u64 v[24:25], v[22:23], 0, v[24:25]
	v_add_u32_e32 v6, s10, v74
	global_store_dwordx4 v[24:25], v[2:5], off
	s_andn2_b64 vcc, exec, s[8:9]
	s_mov_b32 s20, s21
	v_cvt_pk_bf16_f32 v2, v9, v7
	v_ashrrev_i32_e32 v7, 31, v6
	v_cvt_pk_bf16_f32 v3, v11, v13
	v_cvt_pk_bf16_f32 v4, v15, v17
	v_cvt_pk_bf16_f32 v5, v19, v21
	v_lshlrev_b64 v[6:7], 12, v[6:7]
	ds_read2_b32 v[8:9], v77 offset0:49 offset1:57
	ds_read2_b32 v[10:11], v77 offset0:16 offset1:24
	ds_read2_b32 v[12:13], v77 offset0:82 offset1:90
	ds_read2_b32 v[14:15], v77 offset0:115 offset1:123
	ds_read2_b32 v[16:17], v77 offset0:148 offset1:156
	ds_read2_b32 v[18:19], v77 offset0:181 offset1:189
	ds_read2_b32 v[20:21], v77 offset0:214 offset1:222
	ds_read2_b32 v[24:25], v77 offset0:247 offset1:255
	v_lshl_add_u64 v[6:7], v[22:23], 0, v[6:7]
	global_store_dwordx4 v[6:7], v[2:5], off
	v_add_u32_e32 v6, s10, v75
	v_ashrrev_i32_e32 v7, 31, v6
	v_lshlrev_b64 v[6:7], 12, v[6:7]
	s_waitcnt lgkmcnt(6)
	v_cvt_pk_bf16_f32 v2, v10, v8
	s_waitcnt lgkmcnt(4)
	v_cvt_pk_bf16_f32 v3, v12, v14
	s_waitcnt lgkmcnt(2)
	v_cvt_pk_bf16_f32 v4, v16, v18
	s_waitcnt lgkmcnt(0)
	v_cvt_pk_bf16_f32 v5, v20, v24
	v_lshl_add_u64 v[6:7], v[22:23], 0, v[6:7]
	global_store_dwordx4 v[6:7], v[2:5], off
	v_add_u32_e32 v6, s10, v76
	v_ashrrev_i32_e32 v7, 31, v6
	v_lshlrev_b64 v[6:7], 12, v[6:7]
	v_cvt_pk_bf16_f32 v2, v11, v9
	v_cvt_pk_bf16_f32 v3, v13, v15
	v_cvt_pk_bf16_f32 v4, v17, v19
	v_cvt_pk_bf16_f32 v5, v21, v25
	v_lshl_add_u64 v[6:7], v[22:23], 0, v[6:7]
	global_store_dwordx4 v[6:7], v[2:5], off
	s_waitcnt lgkmcnt(0)
	s_waitcnt vmcnt(4)
	v_mov_b32_e32 v6, v34
	v_mov_b32_e32 v7, v35
	v_mov_b32_e32 v2, v30
	v_mov_b32_e32 v3, v31
	v_mov_b32_e32 v4, v32
	v_mov_b32_e32 v5, v33
	v_mov_b32_e32 v8, v36
	v_mov_b32_e32 v9, v37
	v_mov_b32_e32 v10, v26
	v_mov_b32_e32 v11, v27
	v_mov_b32_e32 v12, v28
	v_mov_b32_e32 v13, v29
	v_mov_b32_e32 v14, v46
	v_mov_b32_e32 v15, v47
	v_mov_b32_e32 v16, v48
	v_mov_b32_e32 v17, v49
	v_mov_b32_e32 v18, v54
	v_mov_b32_e32 v19, v55
	v_mov_b32_e32 v20, v56
	v_mov_b32_e32 v21, v57
	v_mov_b32_e32 v22, v58
	v_mov_b32_e32 v23, v59
	v_mov_b32_e32 v24, v60
	v_mov_b32_e32 v25, v61
	v_mov_b32_e32 v38, v50
	v_mov_b32_e32 v39, v51
	v_mov_b32_e32 v40, v52
	v_mov_b32_e32 v41, v53
	v_mov_b32_e32 v42, v62
	v_mov_b32_e32 v43, v63
	v_mov_b32_e32 v44, v64
	v_mov_b32_e32 v45, v65
	s_cbranch_vccz .LBB0_217

.Ltrw_229:
	ds_write2_b32 v79, v2, v3 offset1:1
	ds_write2_b32 v79, v4, v5 offset0:2 offset1:3
	v_add_u32_e32 v2, 0x420, v79
	ds_write2_b32 v2, v6, v7 offset1:1
	v_add_u32_e32 v2, 0x428, v79
	ds_write2_b32 v2, v8, v9 offset1:1
	v_add_u32_e32 v2, 0x840, v79
	ds_write2_b32 v2, v10, v11 offset1:1
	v_add_u32_e32 v2, 0x848, v79
	ds_write2_b32 v2, v12, v13 offset1:1
	v_add_u32_e32 v2, 0xc60, v79
	s_ashr_i32 s4, s16, 31
	ds_write2_b32 v2, v14, v15 offset1:1
	v_add_u32_e32 v2, 0xc68, v79
	s_lshr_b32 s4, s4, 19
	ds_write2_b32 v2, v16, v17 offset1:1
	v_add_u32_e32 v2, 0x1080, v79
	s_add_i32 s5, s16, s4
	ds_write2_b32 v2, v18, v19 offset1:1
	v_add_u32_e32 v2, 0x1088, v79
	s_ashr_i32 s4, s5, 13
	s_and_b32 s5, s5, 0xe000
	ds_write2_b32 v2, v20, v21 offset1:1
	v_add_u32_e32 v2, 0x14a0, v79
	s_sub_i32 s8, s16, s5
	s_ashr_i32 s5, s4, 31
	ds_write2_b32 v2, v22, v23 offset1:1
	v_add_u32_e32 v2, 0x14a8, v79
	s_lshl_b64 s[4:5], s[4:5], 25
	ds_write2_b32 v2, v24, v25 offset1:1
	v_add_u32_e32 v2, 0x18c0, v79
	s_add_u32 s9, s10, s4
	s_sext_i32_i16 s4, s8
	ds_write2_b32 v2, v38, v39 offset1:1
	v_add_u32_e32 v2, 0x18c8, v79
	s_addc_u32 s16, s11, s5
	s_bfe_u32 s4, s4, 0x60019
	ds_write2_b32 v2, v40, v41 offset1:1
	v_add_u32_e32 v2, 0x1ce0, v79
	s_add_i32 s4, s8, s4
	ds_write2_b32 v2, v42, v43 offset1:1
	v_add_u32_e32 v2, 0x1ce8, v79
	s_sext_i32_i16 s5, s4
	s_and_b32 s4, s4, 0xffc0
	ds_write2_b32 v2, v44, v45 offset1:1
	s_sub_i32 s4, s8, s4
	s_waitcnt lgkmcnt(0)
	s_sext_i32_i16 s8, s4
	s_and_b32 s4, s5, 0xffffffc0
	s_ashr_i32 s5, s4, 31
	ds_read2_b32 v[6:7], v77 offset0:33 offset1:41
	ds_read2_b32 v[8:9], v77 offset1:8
	ds_read2_b32 v[10:11], v77 offset0:66 offset1:74
	ds_read2_b32 v[12:13], v77 offset0:99 offset1:107
	ds_read2_b32 v[14:15], v77 offset0:132 offset1:140
	ds_read2_b32 v[16:17], v77 offset0:165 offset1:173
	ds_read2_b32 v[18:19], v77 offset0:198 offset1:206
	ds_read2_b32 v[20:21], v77 offset0:231 offset1:239
	s_lshl_b32 s8, s8, 5
	s_lshl_b64 s[4:5], s[4:5], 1
	s_add_u32 s4, s9, s4
	v_add_u32_e32 v24, s8, v72
	s_addc_u32 s5, s16, s5
	v_ashrrev_i32_e32 v25, 31, v24
	v_lshl_add_u64 v[22:23], s[4:5], 0, v[66:67]
	v_lshlrev_b64 v[24:25], 14, v[24:25]
	s_waitcnt lgkmcnt(6)
	v_cvt_pk_bf16_f32 v2, v8, v6
	s_waitcnt lgkmcnt(4)
	v_cvt_pk_bf16_f32 v3, v10, v12
	s_waitcnt lgkmcnt(2)
	v_cvt_pk_bf16_f32 v4, v14, v16
	s_waitcnt lgkmcnt(0)
	v_cvt_pk_bf16_f32 v5, v18, v20
	v_lshl_add_u64 v[24:25], v[22:23], 0, v[24:25]
	v_add_u32_e32 v6, s8, v74
	global_store_dwordx4 v[24:25], v[2:5], off
	s_andn2_b64 vcc, exec, s[2:3]
	s_mov_b32 s16, s17
	v_cvt_pk_bf16_f32 v2, v9, v7
	v_ashrrev_i32_e32 v7, 31, v6
	v_cvt_pk_bf16_f32 v3, v11, v13
	v_cvt_pk_bf16_f32 v4, v15, v17
	v_cvt_pk_bf16_f32 v5, v19, v21
	v_lshlrev_b64 v[6:7], 14, v[6:7]
	ds_read2_b32 v[8:9], v77 offset0:49 offset1:57
	ds_read2_b32 v[10:11], v77 offset0:16 offset1:24
	ds_read2_b32 v[12:13], v77 offset0:82 offset1:90
	ds_read2_b32 v[14:15], v77 offset0:115 offset1:123
	ds_read2_b32 v[16:17], v77 offset0:148 offset1:156
	ds_read2_b32 v[18:19], v77 offset0:181 offset1:189
	ds_read2_b32 v[20:21], v77 offset0:214 offset1:222
	ds_read2_b32 v[24:25], v77 offset0:247 offset1:255
	v_lshl_add_u64 v[6:7], v[22:23], 0, v[6:7]
	global_store_dwordx4 v[6:7], v[2:5], off
	v_add_u32_e32 v6, s8, v75
	v_ashrrev_i32_e32 v7, 31, v6
	v_lshlrev_b64 v[6:7], 14, v[6:7]
	s_waitcnt lgkmcnt(6)
	v_cvt_pk_bf16_f32 v2, v10, v8
	s_waitcnt lgkmcnt(4)
	v_cvt_pk_bf16_f32 v3, v12, v14
	s_waitcnt lgkmcnt(2)
	v_cvt_pk_bf16_f32 v4, v16, v18
	s_waitcnt lgkmcnt(0)
	v_cvt_pk_bf16_f32 v5, v20, v24
	v_lshl_add_u64 v[6:7], v[22:23], 0, v[6:7]
	global_store_dwordx4 v[6:7], v[2:5], off
	v_add_u32_e32 v6, s8, v76
	v_ashrrev_i32_e32 v7, 31, v6
	v_lshlrev_b64 v[6:7], 14, v[6:7]
	v_cvt_pk_bf16_f32 v2, v11, v9
	v_cvt_pk_bf16_f32 v3, v13, v15
	v_cvt_pk_bf16_f32 v4, v17, v19
	v_cvt_pk_bf16_f32 v5, v21, v25
	v_lshl_add_u64 v[6:7], v[22:23], 0, v[6:7]
	global_store_dwordx4 v[6:7], v[2:5], off
	s_waitcnt lgkmcnt(0)
	s_waitcnt vmcnt(4)
	v_mov_b32_e32 v6, v34
	v_mov_b32_e32 v7, v35
	v_mov_b32_e32 v2, v30
	v_mov_b32_e32 v3, v31
	v_mov_b32_e32 v4, v32
	v_mov_b32_e32 v5, v33
	v_mov_b32_e32 v8, v36
	v_mov_b32_e32 v9, v37
	v_mov_b32_e32 v10, v26
	v_mov_b32_e32 v11, v27
	v_mov_b32_e32 v12, v28
	v_mov_b32_e32 v13, v29
	v_mov_b32_e32 v14, v46
	v_mov_b32_e32 v15, v47
	v_mov_b32_e32 v16, v48
	v_mov_b32_e32 v17, v49
	v_mov_b32_e32 v18, v54
	v_mov_b32_e32 v19, v55
	v_mov_b32_e32 v20, v56
	v_mov_b32_e32 v21, v57
	v_mov_b32_e32 v22, v58
	v_mov_b32_e32 v23, v59
	v_mov_b32_e32 v24, v60
	v_mov_b32_e32 v25, v61
	v_mov_b32_e32 v38, v50
	v_mov_b32_e32 v39, v51
	v_mov_b32_e32 v40, v52
	v_mov_b32_e32 v41, v53
	v_mov_b32_e32 v42, v62
	v_mov_b32_e32 v43, v63
	v_mov_b32_e32 v44, v64
	v_mov_b32_e32 v45, v65
	s_cbranch_vccz .LBB0_239
